# attention row sums via 4-pass v_mfma_f32_16x16x32_bf16 with a masked-ones B operand (4 accumulator regs instead of 16), row sums leave via per-wave LDS scratch
# speedup vs baseline: 1.0282x; 1.0012x over previous
; __device__ __forceinline__ int crow(int r, int hi) { return (r & 3) + 8 * (r >> 2) + 4 * hi; }
; __device__ __forceinline__ int crow(int r,int hi){return (r&3)+8*(r>>2)+4*hi;}
; template<int THRL> __device__ __forceinline__ void attn_unit(int b,int h,int qb,const bf16*Q,const bf16*__restrict__ K,const bf16*__restrict__ V,bf16*O,const unsigned*MASK,char*shm){
;     ...
;   {auto rr=__builtin_amdgcn_permlane32_swap(__float_as_uint(l_reg),__float_as_uint(l_reg),false,false);l_reg=__uint_as_float(rr[0])+__uint_as_float(rr[1]);}
;   if(hi==0)wsf[32+r32]=l_reg;asm volatile("s_waitcnt lgkmcnt(0)":::"memory");
;   float rli[16];
;   #pragma unroll
;   for(int r=0;r<16;++r)rli[r]=__builtin_amdgcn_rcpf(wsf[32+crow(r,hi)]);
;   bf16*Ow=O+(rowbase+q0+wid*QBLK)*OPITCH+h*D;
;   { bf16*stg=(bf16*)(shm+LDS_OST)+wid*2048;
;     #pragma unroll
;     for(int r=0;r<16;++r){const int orow=crow(r,hi);
;       #pragma unroll
;       for(int d0=0;d0<2;++d0)stg[orow*64+d0*32+r32]=__float2bfloat16(o[d0][r]*rli[r]);}
;     asm volatile("s_waitcnt lgkmcnt(0)":::"memory");
;     #pragma unroll
;     for(int i=0;i<4;++i){const int row=i*8+(lane>>3),ch=lane&7; const u32x4 v=*(const u32x4*)(stg+row*64+ch*8); ATTN_STORE16(Ow+(long)row*OPITCH+ch*8,v);} }
;   asm volatile("s_waitcnt lgkmcnt(0)\n\ts_barrier":::"memory");
.LBB0_1258:
	s_andn2_b64 vcc, exec, s[4:5]
	s_cbranch_vccnz .LBB0_1395
	v_and_b32_e32 v228, 63, v0
	v_lshrrev_b32_e32 v229, 4, v228
	v_and_b32_e32 v228, 15, v228
	v_and_b32_e32 v229, 1, v229
	v_cmp_eq_u32_e64 s[4:5], v228, v229
	v_mov_b32_e32 v230, 0x3f803f80
	s_nop 1
	v_cndmask_b32_e64 v204, 0, v230, s[4:5]
	v_mov_b32_e32 v205, v204
	v_mov_b32_e32 v206, v204
	v_mov_b32_e32 v207, v204
	s_mov_b32 s32, 4
	v_lshrrev_b32_e32 v228, 1, v0
	v_and_b32_e32 v229, 1, v0
	v_lshlrev_b32_e32 v230, 2, v229
	v_lshrrev_b32_e32 v231, v230, v228
	v_bfe_i32 v232, v231, 0, 1
	v_bfe_i32 v233, v231, 1, 1
	v_and_b32_e32 v232, 0xffff, v232
	v_and_b32_e32 v233, 0xffff0000, v233
	v_or_b32_e32 v232, v232, v233
	v_bfe_i32 v233, v231, 2, 1
	v_bfe_i32 v234, v231, 3, 1
	v_and_b32_e32 v233, 0xffff, v233
	v_and_b32_e32 v234, 0xffff0000, v234
	v_or_b32_e32 v233, v233, v234
	v_lshlrev_b32_e32 v234, 3, v0
	ds_write_b64 v234, v[232:233] offset:51200
	v_mov_b32_e32 v1, v0
	s_mov_b64 s[4:5], s[66:67]
	s_load_dwordx2 s[4:5], s[4:5], 0xd0
	v_readlane_b32 s6, v252, 16
	v_readlane_b32 s7, v252, 17
	s_mov_b32 s55, 0
	s_waitcnt lgkmcnt(0)
	s_add_u32 s8, s4, 0xea00000
	s_addc_u32 s9, s5, 0
	s_add_u32 s17, s4, 0x10a00000
	s_addc_u32 s18, s5, 0
	s_add_u32 s19, s4, 0x12a00000
	s_addc_u32 s20, s5, 0
	s_add_u32 s21, s4, 0x15f00400
	s_addc_u32 s22, s5, 0
	s_add_u32 s23, s4, s6
	s_addc_u32 s54, s5, s7
	s_branch .LBB0_1262
.LBB0_1260:
	s_or_b64 exec, exec, s[4:5]
	s_waitcnt lgkmcnt(0)
	ds_read_b128 v[36:39], v52 offset:49280
	ds_read_b128 v[40:43], v52 offset:49312
	s_lshl_b64 s[4:5], s[44:45], 11
	s_add_u32 s4, s21, s4
	s_addc_u32 s5, s22, s5
	s_waitcnt lgkmcnt(1)
	v_rcp_f32_e32 v2, v36
	v_rcp_f32_e32 v44, v37
	s_lshl_b32 s7, s7, 12
	v_rcp_f32_e32 v45, v38
	v_rcp_f32_e32 v46, v39
	s_waitcnt lgkmcnt(0)
	v_rcp_f32_e32 v47, v40
	ds_read_b128 v[36:39], v52 offset:49344
	v_rcp_f32_e32 v48, v41
	v_rcp_f32_e32 v49, v42
	v_rcp_f32_e32 v50, v43
	ds_read_b128 v[40:43], v52 offset:49376
	s_add_i32 s7, s7, 0
	v_lshlrev_b32_e32 v51, 9, v214
	v_lshlrev_b32_e32 v52, 1, v213
	v_mul_f32_e32 v20, v20, v2
	v_mul_f32_e32 v2, v4, v2
	v_add3_u32 v51, s7, v51, v52
	v_cvt_pk_bf16_f32 v2, v2, s0
	ds_write_b16 v51, v2 offset:55360
	v_mul_f32_e32 v2, v21, v44
	v_cvt_pk_bf16_f32 v2, v2, s0
	ds_write_b16 v51, v2 offset:55424
	v_mul_f32_e32 v2, v5, v44
	v_cvt_pk_bf16_f32 v2, v2, s0
	ds_write_b16 v51, v2 offset:55488
	v_mul_f32_e32 v2, v22, v45
	v_cvt_pk_bf16_f32 v2, v2, s0
	ds_write_b16 v51, v2 offset:55552
	v_mul_f32_e32 v2, v6, v45
	v_cvt_pk_bf16_f32 v2, v2, s0
	ds_write_b16 v51, v2 offset:55616
	v_mul_f32_e32 v2, v23, v46
	v_cvt_pk_bf16_f32 v2, v2, s0
	ds_write_b16 v51, v2 offset:55680
	v_mul_f32_e32 v2, v7, v46
	v_cvt_pk_bf16_f32 v2, v2, s0
	ds_write_b16 v51, v2 offset:55744
	v_mul_f32_e32 v2, v24, v47
	v_cvt_pk_bf16_f32 v2, v2, s0
	ds_write_b16 v51, v2 offset:56320
	v_mul_f32_e32 v2, v8, v47
	v_cvt_pk_bf16_f32 v2, v2, s0
	ds_write_b16 v51, v2 offset:56384
	v_mul_f32_e32 v2, v25, v48
	v_cvt_pk_bf16_f32 v2, v2, s0
	ds_write_b16 v51, v2 offset:56448
	v_mul_f32_e32 v2, v9, v48
	v_cvt_pk_bf16_f32 v2, v2, s0
	ds_write_b16 v51, v2 offset:56512
	v_mul_f32_e32 v2, v26, v49
	v_cvt_pk_bf16_f32 v2, v2, s0
	ds_write_b16 v51, v2 offset:56576
	v_mul_f32_e32 v2, v10, v49
	v_cvt_pk_bf16_f32 v2, v2, s0
	s_waitcnt lgkmcnt(13)
	v_rcp_f32_e32 v36, v36
	ds_write_b16 v51, v2 offset:56640
	v_mul_f32_e32 v2, v27, v50
	v_cvt_pk_bf16_f32 v2, v2, s0
	ds_write_b16 v51, v2 offset:56704
	v_mul_f32_e32 v2, v11, v50
	v_cvt_pk_bf16_f32 v2, v2, s0
	v_rcp_f32_e32 v37, v37
	ds_write_b16 v51, v2 offset:56768
	v_mul_f32_e32 v2, v28, v36
	v_cvt_pk_bf16_f32 v2, v2, s0
	ds_write_b16 v51, v2 offset:57344
	v_mul_f32_e32 v2, v12, v36
	v_cvt_pk_bf16_f32 v2, v2, s0
	v_rcp_f32_e32 v38, v38
	ds_write_b16 v51, v2 offset:57408
	v_mul_f32_e32 v2, v29, v37
	v_cvt_pk_bf16_f32 v2, v2, s0
	ds_write_b16 v51, v2 offset:57472
	v_mul_f32_e32 v2, v13, v37
	v_cvt_pk_bf16_f32 v2, v2, s0
	v_rcp_f32_e32 v39, v39
	ds_write_b16 v51, v2 offset:57536
	v_mul_f32_e32 v2, v30, v38
	v_cvt_pk_bf16_f32 v2, v2, s0
	ds_write_b16 v51, v2 offset:57600
	v_mul_f32_e32 v2, v14, v38
	v_cvt_pk_bf16_f32 v2, v2, s0
	s_waitcnt lgkmcnt(14)
	v_rcp_f32_e32 v40, v40
	ds_write_b16 v51, v2 offset:57664
	v_mul_f32_e32 v2, v31, v39
	v_cvt_pk_bf16_f32 v2, v2, s0
	ds_write_b16 v51, v2 offset:57728
	v_mul_f32_e32 v2, v15, v39
	v_cvt_pk_bf16_f32 v2, v2, s0
	v_rcp_f32_e32 v41, v41
	ds_write_b16 v51, v2 offset:57792
	v_mul_f32_e32 v2, v32, v40
	v_cvt_pk_bf16_f32 v2, v2, s0
	ds_write_b16 v51, v2 offset:58368
	v_mul_f32_e32 v2, v16, v40
	v_cvt_pk_bf16_f32 v2, v2, s0
	v_rcp_f32_e32 v42, v42
	ds_write_b16 v51, v2 offset:58432
	v_mul_f32_e32 v2, v33, v41
	v_cvt_pk_bf16_f32 v2, v2, s0
	ds_write_b16 v51, v2 offset:58496
	v_mul_f32_e32 v2, v17, v41
	v_cvt_pk_bf16_f32 v2, v2, s0
	v_rcp_f32_e32 v43, v43
	ds_write_b16 v51, v2 offset:58560
	v_mul_f32_e32 v2, v34, v42
	v_cvt_pk_bf16_f32 v2, v2, s0
	ds_write_b16 v51, v2 offset:58624
	v_mul_f32_e32 v2, v18, v42
	v_cvt_pk_bf16_f32 v2, v2, s0
	ds_write_b16 v51, v2 offset:58688
	v_mul_f32_e32 v2, v35, v43
	v_cvt_pk_bf16_f32 v2, v2, s0
	ds_write_b16 v51, v2 offset:58752
	v_mul_f32_e32 v2, v19, v43
	v_cvt_pk_bf16_f32 v2, v2, s0
	ds_write_b16 v51, v2 offset:58816
	v_lshlrev_b32_e32 v2, 1, v212
	v_cvt_pk_bf16_f32 v20, v20, s0
	s_add_u32 s4, s4, s38
	v_and_b32_e32 v2, 0x70, v2
	ds_write_b16 v51, v20 offset:55296
	s_addc_u32 s5, s5, s39
	v_lshrrev_b32_e32 v1, 3, v1
	v_add_u32_e32 v16, s7, v2
	s_waitcnt lgkmcnt(0)
	v_lshl_add_u64 v[12:13], s[4:5], 0, v[2:3]
	v_lshl_add_u32 v2, v1, 7, v16
	v_or_b32_e32 v17, 8, v1
	ds_read_b128 v[4:7], v2 offset:55296
	v_lshl_add_u32 v8, v17, 7, v16
	ds_read_b128 v[8:11], v8 offset:55296
	v_lshlrev_b32_e32 v2, 11, v1
	v_lshl_add_u64 v[14:15], v[12:13], 0, v[2:3]
	v_lshlrev_b32_e32 v2, 11, v17
	s_waitcnt lgkmcnt(1)
	global_store_dwordx4 v[14:15], v[4:7], off
	s_add_i32 s55, s55, 1
	s_mov_b64 s[4:5], 0
	v_lshl_add_u64 v[4:5], v[12:13], 0, v[2:3]
	v_or_b32_e32 v2, 16, v1
	s_waitcnt lgkmcnt(0)
	global_store_dwordx4 v[4:5], v[8:11], off
	v_lshl_add_u32 v4, v2, 7, v16
	v_or_b32_e32 v1, 24, v1
	ds_read_b128 v[4:7], v4 offset:55296
	v_lshl_add_u32 v8, v1, 7, v16
	ds_read_b128 v[8:11], v8 offset:55296
	v_lshlrev_b32_e32 v2, 11, v2
	v_lshl_add_u64 v[14:15], v[12:13], 0, v[2:3]
	v_lshlrev_b32_e32 v2, 11, v1
	s_waitcnt lgkmcnt(1)
	global_store_dwordx4 v[14:15], v[4:7], off
	s_nop 1
	v_lshl_add_u64 v[4:5], v[12:13], 0, v[2:3]
	s_waitcnt lgkmcnt(0)
	global_store_dwordx4 v[4:5], v[8:11], off
	s_waitcnt lgkmcnt(0)
	s_barrier

;   #define DMA_K(t,slot) glds16(ksrc+(long)(t)*KVBLK*DM,(unsigned)__builtin_amdgcn_readfirstlane(kdst+(slot)))
;   #define DMA_V(t,slot) glds16(vsrc+(long)(t)*KVBLK*DM,(unsigned)__builtin_amdgcn_readfirstlane(vdst+(slot)))
;   #define WLOAD(W,t) asm volatile("global_load_dword %0, %1, off":"=v"(W):"v"(mwl+(size_t)(t)*64):"memory")
; template<int THRL> __device__ __forceinline__ void attn_unit(int b,int h,int qb,const bf16*Q,const bf16*__restrict__ K,const bf16*__restrict__ V,bf16*O,const unsigned*MASK,char*shm){
;   int tid_=threadIdx.x; asm volatile("":"+v"(tid_));
;   const int tid=tid_,lane=tid&63,r32=lane&31,hi=lane>>5; const int wid=__builtin_amdgcn_readfirstlane(tid>>6);
;   const long rowbase=(long)b*SEQ; const int q0=qb*QB;
;   const bf16*Qw=Q+(rowbase+q0+wid*QBLK)*DM+h*D;
;   const bf16*Kh=K+rowbase*DM+h*D,*Vh=V+rowbase*DM+h*D;
;   const unsigned lds0=(unsigned)(uintptr_t)shm;
;   float*wsf=(float*)(shm+LDS_WS)+wid*64;
;   const bf16*ksrc=Kh+(long)lane*DM+wid*8;
;   const bf16*vsrc=Vh+(long)(16*(wid&3)+(lane>>2))*DM+(wid>>2)*32+(lane&3)*8;
;   const unsigned kdst=lds0+LDS_K+wid*1024, vdst=lds0+LDS_V+wid*1024;
;     ...
;   const int vb0=(int)(lds0+LDS_V)+((lane>>4)&1)*32+(lane&3)*8+(4*hi+((lane&15)>>2))*64;
;   const char*Kbase=shm+LDS_K; bf16x8 kf[8];
;   const lds_cptr shm3=(lds_cptr)shm; const lds_cptr kp0=shm3+LDS_K+hi*1024+r32*16; const lds_cptr vp0=shm3+LDS_V+((lane>>4)&1)*32+(lane&3)*8+(4*hi+((lane&15)>>2))*64;
;   const int NT=(q0+QB)/KVBLK;
;   const unsigned*mwl=MASK+((size_t)(b*256+qb*8+wid)*128)*64+lane;
;   unsigned wA,wB;
;     ...
;   WLOAD(wA,0);WLOAD(wB,1);
;   DMA_K(0,0);DMA_V(0,0);DMA_K(1,SLOTB);
;   bf16x8 qr[4];
;   #pragma unroll
;   for(int d0=0;d0<4;++d0)qr[d0]=*reinterpret_cast<const bf16x8*>(&Qw[(long)r32*DM+d0*16+hi*8]);
;   float mhat=0.f,l_reg=0.f;f32x16 o[2];o[0]=f32x16{};o[1]=f32x16{};f32x16 negm=f32x16{};asm volatile("":"+v"(negm));
.LBB0_1271:
	s_ashr_i32 s4, s6, 31
	s_lshr_b32 s4, s4, 29
	s_add_i32 s4, s6, s4
	s_ashr_i32 s42, s4, 3
	v_mov_b32_e32 v58, v0
	s_and_b32 s4, s4, 0x3fffff8
	s_ashr_i32 s43, s42, 31
	v_readfirstlane_b32 s50, v58
	s_lshl_b32 s51, s56, 8
	s_sub_i32 s38, s6, s4
	s_ashr_i32 s7, s50, 6
	s_lshl_b64 s[4:5], s[42:43], 13
	s_ashr_i32 s39, s51, 31
	s_add_u32 s4, s4, s51
	s_addc_u32 s5, s5, s39
	s_lshl_b32 s39, s7, 5
	s_ashr_i32 s40, s39, 31
	s_add_u32 s44, s4, s39
	s_addc_u32 s45, s5, s40
	s_lshl_b64 s[4:5], s[44:45], 10
	s_add_u32 s40, s8, s4
	s_addc_u32 s41, s9, s5
	s_lshl_b32 s4, s38, 6
	s_ashr_i32 s5, s4, 31
	s_lshl_b64 s[38:39], s[4:5], 1
	s_add_u32 s40, s40, s38
	s_addc_u32 s41, s41, s39
	s_lshl_b64 s[4:5], s[42:43], 23
	s_add_u32 s43, s17, s4
	s_addc_u32 s47, s18, s5
	s_add_u32 s46, s43, s38
	s_addc_u32 s47, s47, s39
	s_add_u32 s4, s19, s4
	v_and_b32_e32 v1, 63, v58
	s_addc_u32 s5, s20, s5
	s_add_u32 s48, s4, s38
	v_lshlrev_b32_e32 v2, 10, v1
	s_addc_u32 s49, s5, s39
	v_lshl_add_u64 v[4:5], s[46:47], 0, v[2:3]
	s_lshl_b32 s46, s7, 3
	s_lshl_b32 s4, s7, 4
	v_bfe_u32 v2, v58, 2, 4
	s_ashr_i32 s47, s46, 31
	v_and_or_b32 v2, s4, 48, v2
	s_ashr_i32 s4, s50, 3
	v_lshl_add_u64 v[194:195], s[46:47], 1, v[4:5]
	s_and_b32 s46, s4, 0xffffffe0
	s_and_b32 s5, s50, 0x3fffffc0
	s_ashr_i32 s47, s46, 31
	s_lshl_b32 s58, s7, 10
	s_cmp_lg_u32 0, -1
	s_cselect_b32 s4, 0, 0
	s_lshl_b32 s42, s42, 8
	s_lshl_b32 s43, s56, 3
	s_add_i32 s42, s42, s43
	s_add_i32 s42, s42, s7
	v_lshlrev_b32_e32 v2, 10, v2
	v_lshlrev_b32_e32 v212, 3, v58
	s_add_i32 s58, s58, s4
	s_ashr_i32 s43, s42, 31
	v_lshl_add_u64 v[4:5], s[48:49], 0, v[2:3]
	v_and_b32_e32 v215, 24, v212
	s_add_i32 s59, s58, 0x6000
	s_add_i32 s4, s51, 0x100
	s_lshl_b64 s[42:43], s[42:43], 15
	v_lshl_add_u64 v[4:5], s[46:47], 1, v[4:5]
	v_lshlrev_b32_e32 v2, 1, v215
	s_add_u32 s42, s23, s42
	v_lshl_add_u64 v[208:209], v[4:5], 0, v[2:3]
	s_addc_u32 s43, s54, s43
	v_lshlrev_b32_e32 v2, 2, v1
	v_lshl_add_u64 v[84:85], s[42:43], 0, v[2:3]
	global_load_dword v59, v[84:85], off
	s_waitcnt vmcnt(0)
	v_lshlrev_b32_sdwa v225, s32, v59 dst_sel:DWORD dst_unused:UNUSED_PAD src0_sel:DWORD src1_sel:BYTE_0
	v_lshlrev_b32_sdwa v226, s32, v59 dst_sel:DWORD dst_unused:UNUSED_PAD src0_sel:DWORD src1_sel:BYTE_1
	v_lshlrev_b32_sdwa v248, s32, v59 dst_sel:DWORD dst_unused:UNUSED_PAD src0_sel:DWORD src1_sel:BYTE_2
	v_lshlrev_b32_sdwa v249, s32, v59 dst_sel:DWORD dst_unused:UNUSED_PAD src0_sel:DWORD src1_sel:BYTE_3
	v_lshl_add_u64 v[186:187], v[84:85], 0, s[30:31]
	global_load_dword v218, v[186:187], off
	v_and_b32_e32 v213, 31, v58
	s_mov_b32 s42, m0
	s_mov_b32 m0, s58
	s_nop 0
	global_load_lds_dwordx4 v[194:195], off
	s_mov_b32 m0, s42
	v_bfe_u32 v214, v58, 5, 1
	s_mov_b32 s42, m0
	s_mov_b32 m0, s59
	s_nop 0
	global_load_lds_dwordx4 v[208:209], off
	s_mov_b32 m0, s42
	v_lshlrev_b32_e32 v2, 10, v213
	v_lshl_add_u64 v[4:5], v[194:195], 0, s[36:37]
	s_add_i32 s42, s58, 0x2000
	s_mov_b32 s43, m0
	s_mov_b32 m0, s42
	s_nop 0
	global_load_lds_dwordx4 v[4:5], off
	s_mov_b32 m0, s43
	v_lshl_or_b32 v2, v214, 4, v2
	global_load_dwordx4 v[138:141], v2, s[40:41]
	global_load_dwordx4 v[134:137], v2, s[40:41] offset:32
	global_load_dwordx4 v[126:129], v2, s[40:41] offset:64
	global_load_dwordx4 v[122:125], v2, s[40:41] offset:96
	v_mov_b32_e32 v228, 0
	v_mov_b32_e32 v229, 0
	v_mov_b32_e32 v230, 0
	v_mov_b32_e32 v231, 0
	v_mov_b32_e32 v16, v3
	v_mov_b32_e32 v17, v3
	v_lshlrev_b32_e32 v2, 10, v214
	v_lshlrev_b32_e32 v18, 4, v213
	v_mov_b32_e32 v4, v3
	v_mov_b32_e32 v5, v3
	v_mov_b32_e32 v6, v3
	v_mov_b32_e32 v7, v3
	v_mov_b32_e32 v8, v3
	v_mov_b32_e32 v9, v3
	v_mov_b32_e32 v10, v3
	v_mov_b32_e32 v11, v3
	v_mov_b32_e32 v12, v3
	v_mov_b32_e32 v13, v3
	v_mov_b32_e32 v14, v3
	v_mov_b32_e32 v15, v3
	v_add3_u32 v221, 0, v2, v18
	v_mov_b32_e32 v2, v3
	v_mov_b64_e32 v[32:33], v[16:17]
	v_mov_b64_e32 v[30:31], v[14:15]
	v_mov_b64_e32 v[28:29], v[12:13]
	v_mov_b64_e32 v[26:27], v[10:11]
	v_mov_b64_e32 v[24:25], v[8:9]
	v_mov_b64_e32 v[22:23], v[6:7]
	v_mov_b64_e32 v[20:21], v[4:5]
	v_mov_b64_e32 v[18:19], v[2:3]
	v_lshl_add_u64 v[34:35], v[194:195], 0, s[0:1]
	s_add_i32 s40, s58, 0x4000
	s_mov_b32 s41, m0
	s_mov_b32 m0, s40
	s_nop 0
	global_load_lds_dwordx4 v[34:35], off
	s_mov_b32 m0, s41
	s_waitcnt vmcnt(3) lgkmcnt(0)
	s_barrier
; __device__ __forceinline__ void qkt(f32x16&p0,f32x16&p1,const char*Kslot,const bf16x8*qr,const f32x16&negm,int r32,int hi){
;   const char*kb=Kslot+hi*1024+r32*16;
;   #pragma unroll
;   for(int d0=0;d0<4;++d0){
;     const bf16x8 b0=*reinterpret_cast<const bf16x8*>(kb+d0*2048);
;     const bf16x8 b1=*reinterpret_cast<const bf16x8*>(kb+d0*2048+512);
;     if(d0==0){p0=__builtin_amdgcn_mfma_f32_32x32x16_bf16(b0,qr[0],negm,0,0,0);p1=__builtin_amdgcn_mfma_f32_32x32x16_bf16(b1,qr[0],negm,0,0,0);}
;     else{p0=__builtin_amdgcn_mfma_f32_32x32x16_bf16(b0,qr[d0],p0,0,0,0);p1=__builtin_amdgcn_mfma_f32_32x32x16_bf16(b1,qr[d0],p1,0,0,0);}}
; }
; __device__ __forceinline__ void kload8(bf16x8*kf,lds_cptr kp){
;   kf[0]=*(const __attribute__((address_space(3))) bf16x8*)(kp);      kf[1]=*(const __attribute__((address_space(3))) bf16x8*)(kp+512);
;   kf[2]=*(const __attribute__((address_space(3))) bf16x8*)(kp+2048); kf[3]=*(const __attribute__((address_space(3))) bf16x8*)(kp+2560);
;   kf[4]=*(const __attribute__((address_space(3))) bf16x8*)(kp+4096); kf[5]=*(const __attribute__((address_space(3))) bf16x8*)(kp+4608);
;   kf[6]=*(const __attribute__((address_space(3))) bf16x8*)(kp+6144); kf[7]=*(const __attribute__((address_space(3))) bf16x8*)(kp+6656);
; }
; __device__ __forceinline__ void kload2(bf16x8*kf,lds_cptr kp,int j){ kf[2*j]=*(const __attribute__((address_space(3))) bf16x8*)(kp+j*2048); kf[2*j+1]=*(const __attribute__((address_space(3))) bf16x8*)(kp+j*2048+512); }
; __device__ __forceinline__ s16x4 vtr(lds_cptr p){ return __builtin_bit_cast(s16x4,__builtin_amdgcn_ds_read_tr16_b64_v4i16((__attribute__((address_space(3))) v4i16_t*)p)); }
; __device__ __forceinline__ float rowmax(const f32x16&p0,const f32x16&p1){
; template<int THRL> __device__ __forceinline__ void attn_unit(int b,int h,int qb,const bf16*Q,const bf16*__restrict__ K,const bf16*__restrict__ V,bf16*O,const unsigned*MASK,char*shm){
;     ...
;   f32x16 pA0,pA1,pB0,pB1;
;   int sl_prev=0,sl_cur=0,sl_next=SLOTB;
;     ...
;   DMA_K(2,2*SLOTB);
;   WAIT_BAR(3);
;   qkt(pA0,pA1,Kbase,qr,negm,r32,hi);asm volatile("s_nop 15\n\ts_nop 7":"+v"(pA0),"+v"(pA1));
;   START(pA0,pA1);
;   _Pragma("unroll") for(int r=0;r<16;++r)pA1[r]=__builtin_amdgcn_exp2f(pA1[r]);
;   _Pragma("unroll") for(int r=0;r<16;++r){pA0[r]=MASK1(pA0[r],wA,r);pA1[r]=MASK1(pA1[r],wA,16+r);}
	ds_read_b128 v[50:53], v221
	ds_read_b128 v[54:57], v221 offset:512
	s_mov_b32 s40, 0xf149f2ca
	s_waitcnt vmcnt(3) lgkmcnt(1)
	v_mfma_f32_32x32x16_bf16 v[34:49], v[50:53], v[138:141], v[18:33]
	v_bfe_i32 v70, v59, 3, 1
	v_bfe_i32 v71, v59, 4, 1
	v_bfe_i32 v72, v59, 5, 1
	v_bfe_i32 v73, v59, 6, 1
	v_bfe_i32 v74, v59, 7, 1
	v_bfe_i32 v75, v59, 8, 1
	v_bfe_i32 v76, v59, 9, 1
	s_waitcnt lgkmcnt(0)
	v_mfma_f32_32x32x16_bf16 v[18:33], v[54:57], v[138:141], v[18:33]
	ds_read_b128 v[50:53], v221 offset:2048
	ds_read_b128 v[54:57], v221 offset:2560
	v_bfe_i32 v77, v59, 10, 1
	v_bfe_i32 v78, v59, 11, 1
	v_bfe_i32 v79, v59, 12, 1
	v_bfe_i32 v80, v59, 13, 1
	v_bfe_i32 v81, v59, 14, 1
	v_bfe_i32 v82, v59, 15, 1
	s_waitcnt vmcnt(2) lgkmcnt(1)
	v_mfma_f32_32x32x16_bf16 v[34:49], v[50:53], v[134:137], v[34:49]
	s_lshl_b32 s5, s5, 2
	v_bfe_i32 v86, v59, 16, 1
	v_bfe_i32 v87, v59, 17, 1
	v_bfe_i32 v69, v59, 2, 1
	s_ashr_i32 s61, s4, 6
	s_add_i32 s57, s5, 0
	v_lshrrev_b32_e32 v236, 4, v1
	v_and_b32_e32 v237, 1, v1
	v_lshlrev_b32_e32 v236, 4, v236
	v_lshl_add_u32 v236, v237, 6, v236
	v_add_u32_e32 v236, s57, v236
	v_bfe_i32 v67, v59, 0, 1
	s_waitcnt lgkmcnt(0)
	v_mfma_f32_32x32x16_bf16 v[18:33], v[54:57], v[134:137], v[18:33]
	ds_read_b128 v[50:53], v221 offset:4096
	ds_read_b128 v[54:57], v221 offset:4608
	v_bfe_i32 v68, v59, 1, 1
	s_mov_b32 s92, 1
	s_mov_b32 s48, 0
	s_movk_i32 s60, 0x2000
	s_movk_i32 s62, 0x4000
	v_bfe_i32 v88, v59, 18, 1
	s_waitcnt vmcnt(1) lgkmcnt(1)
	v_mfma_f32_32x32x16_bf16 v[34:49], v[50:53], v[126:129], v[34:49]
	ds_read_b128 v[50:53], v221 offset:6144
	v_bfe_i32 v89, v59, 19, 1
	v_bfe_i32 v90, v59, 20, 1
	v_bfe_i32 v91, v59, 21, 1
	v_bfe_i32 v92, v59, 22, 1
	v_bfe_i32 v93, v59, 23, 1
	v_bfe_i32 v94, v59, 24, 1
	s_waitcnt lgkmcnt(1)
	v_mfma_f32_32x32x16_bf16 v[18:33], v[54:57], v[126:129], v[18:33]
	ds_read_b128 v[54:57], v221 offset:6656
	v_bfe_i32 v95, v59, 25, 1
	v_bfe_i32 v96, v59, 26, 1
	v_bfe_i32 v97, v59, 27, 1
	v_bfe_i32 v98, v59, 28, 1
	v_bfe_i32 v99, v59, 29, 1
	v_bfe_i32 v100, v59, 30, 1
	s_waitcnt vmcnt(0) lgkmcnt(1)
	v_mfma_f32_32x32x16_bf16 v[34:49], v[50:53], v[122:125], v[34:49]
	v_lshlrev_b32_e32 v50, 1, v58
	v_lshlrev_b32_e32 v51, 4, v58
	v_and_b32_e32 v217, 32, v50
	v_and_b32_e32 v50, 0xc0, v51
	v_lshl_or_b32 v216, v214, 8, v50
	v_add_u32_e32 v50, 0, v217
	v_add3_u32 v220, v50, v215, v216
	s_waitcnt lgkmcnt(0)
	v_mfma_f32_32x32x16_bf16 v[18:33], v[54:57], v[122:125], v[18:33]
	s_nop 15
	s_nop 7
	s_nop 0
	v_max3_f32 v50, v34, v35, v18
	v_max3_f32 v51, v36, v37, v19
	s_nop 0
	v_max3_f32 v50, v50, v20, v21
	v_max3_f32 v51, v51, v40, v41
	s_nop 0
	v_max3_f32 v50, v50, v38, v39
	v_max3_f32 v51, v51, v24, v25
	s_nop 0
	v_max3_f32 v50, v50, v22, v23
	v_max3_f32 v51, v51, v44, v45
	s_nop 0
	v_max3_f32 v50, v50, v42, v43
	v_max3_f32 v51, v51, v28, v29
	s_nop 0
	v_max3_f32 v50, v50, v26, v27
	v_max3_f32 v51, v51, v48, v49
	s_nop 0
	v_max3_f32 v50, v50, v46, v47
	v_max3_f32 v51, v51, v32, v33
	s_nop 0
	v_max3_f32 v50, v50, v30, v31
	s_nop 0
	v_max_f32_e32 v50, v50, v51
	s_nop 0
	v_mov_b32_e32 v51, v50
	s_nop 1
	v_permlane32_swap_b32_e32 v50, v51
	v_max_f32_e32 v50, v50, v51
	s_nop 0
	v_cmp_lt_f32_e32 vcc, s40, v50
	v_cmp_gt_u32_e64 s[40:41], 32, v1
	s_nop 0
	v_cndmask_b32_e32 v50, 0, v50, vcc
	v_sub_f32_e32 v18, v18, v50
	v_sub_f32_e32 v19, v19, v50
	v_sub_f32_e32 v52, v36, v50
	v_sub_f32_e32 v53, v37, v50
	v_sub_f32_e32 v54, v38, v50
	v_sub_f32_e32 v55, v39, v50
	v_sub_f32_e32 v56, v40, v50
	v_sub_f32_e32 v57, v41, v50
	v_sub_f32_e32 v58, v42, v50
	v_sub_f32_e32 v60, v43, v50
	v_sub_f32_e32 v61, v44, v50
	v_sub_f32_e32 v62, v45, v50
	v_sub_f32_e32 v63, v46, v50
	v_sub_f32_e32 v64, v47, v50
	v_sub_f32_e32 v65, v48, v50
	v_sub_f32_e32 v66, v49, v50
	s_nop 0
	v_exp_f32_e32 v52, v52
	v_exp_f32_e32 v53, v53
	v_exp_f32_e32 v54, v54
	v_exp_f32_e32 v55, v55
	v_exp_f32_e32 v56, v56
	v_exp_f32_e32 v57, v57
	v_exp_f32_e32 v58, v58
	v_exp_f32_e32 v60, v60
	v_exp_f32_e32 v61, v61
	v_exp_f32_e32 v62, v62
	v_exp_f32_e32 v63, v63
	v_exp_f32_e32 v64, v64
	v_exp_f32_e32 v65, v65
	v_exp_f32_e32 v66, v66
	v_exp_f32_e32 v18, v18
	v_exp_f32_e32 v19, v19
	v_add_f32_e32 v219, v3, v50
	v_sub_f32_e32 v34, v34, v50
	v_sub_f32_e32 v35, v35, v50
	v_sub_f32_e32 v20, v20, v50
	v_sub_f32_e32 v21, v21, v50
	v_sub_f32_e32 v22, v22, v50
	s_nop 0
	v_xor_b32_e32 v36, 0x80000000, v219
	v_sub_f32_e32 v23, v23, v50
	v_sub_f32_e32 v24, v24, v50
	v_sub_f32_e32 v25, v25, v50
	v_sub_f32_e32 v26, v26, v50
	v_sub_f32_e32 v27, v27, v50
	v_sub_f32_e32 v28, v28, v50
	v_sub_f32_e32 v29, v29, v50
	v_sub_f32_e32 v30, v30, v50
	v_sub_f32_e32 v31, v31, v50
	v_sub_f32_e32 v32, v32, v50
	v_sub_f32_e32 v33, v33, v50
	v_mov_b32_e32 v37, v36
	v_mov_b32_e32 v38, v36
	v_mov_b32_e32 v39, v36
	v_mov_b32_e32 v40, v36
	v_mov_b32_e32 v41, v36
	v_mov_b32_e32 v42, v36
	v_mov_b32_e32 v43, v36
	v_mov_b32_e32 v44, v36
	v_mov_b32_e32 v45, v36
	v_mov_b32_e32 v46, v36
	v_mov_b32_e32 v47, v36
	v_mov_b32_e32 v48, v36
	v_mov_b32_e32 v49, v36
	v_mov_b32_e32 v50, v36
	v_mov_b32_e32 v51, v36
	s_waitcnt vmcnt(0) lgkmcnt(0)
	s_barrier
; #define MASK1(p,w,e) ({ unsigned m_; asm("v_bfe_i32 %0, %1, %2, 1":"=v"(m_):"v"(w),"n"(e)); __uint_as_float(__float_as_uint(p)&m_); })
; #define WAIT_BAR(N) asm volatile("s_waitcnt vmcnt(" #N ") lgkmcnt(0)\n\ts_barrier":::"memory")
;   #define DMA_K(t,slot) glds16(ksrc+(long)(t)*KVBLK*DM,(unsigned)__builtin_amdgcn_readfirstlane(kdst+(slot)))
;   #define DMA_V(t,slot) glds16(vsrc+(long)(t)*KVBLK*DM,(unsigned)__builtin_amdgcn_readfirstlane(vdst+(slot)))
;   #define ROT() do{sl_prev=sl_cur;sl_cur=sl_next;sl_next=(sl_next==(NSLOT-1)*SLOTB)?0:sl_next+SLOTB;}while(0)
; template<int THRL> __device__ __forceinline__ void attn_unit(int b,int h,int qb,const bf16*Q,const bf16*__restrict__ K,const bf16*__restrict__ V,bf16*O,const unsigned*MASK,char*shm){
;     ...
;   _Pragma("unroll") for(int r=0;r<16;++r){pA0[r]=MASK1(pA0[r],wA,r);pA1[r]=MASK1(pA1[r],wA,16+r);}
;   WAIT_BAR(0);
;   DMA_K(3,0);DMA_V(1,SLOTB);
;   ROT();
;   kload8(kf,kp0+sl_cur);
;   WAIT_BAR(2);
;   s16x4 vlo[8],vhi[8]; u32x4 pw0,pw1,pw2,pw3;
	v_and_b32_e32 v83, v82, v66
	v_and_b32_e32 v82, v81, v65
	v_and_b32_e32 v81, v80, v64
	v_and_b32_e32 v80, v79, v63
	v_and_b32_e32 v79, v78, v62
	v_and_b32_e32 v78, v77, v61
	v_and_b32_e32 v77, v76, v60
	v_and_b32_e32 v76, v75, v58
	v_and_b32_e32 v75, v74, v57
	v_and_b32_e32 v74, v73, v56
	v_and_b32_e32 v73, v72, v55
	v_and_b32_e32 v72, v71, v54
	v_and_b32_e32 v71, v70, v53
	v_and_b32_e32 v70, v69, v52
	v_and_b32_e32 v53, v87, v19
	v_and_b32_e32 v52, v86, v18
	v_lshl_add_u64 v[18:19], v[194:195], 0, s[82:83]
	s_mov_b32 s4, m0
	s_mov_b32 m0, s58
	s_nop 0
	global_load_lds_dwordx4 v[18:19], off
	s_mov_b32 m0, s4
	v_lshl_add_u64 v[18:19], v[208:209], 0, s[36:37]
	s_add_i32 s4, s58, 0x8000
	s_mov_b32 s5, m0
	s_mov_b32 m0, s4
	s_nop 0
	global_load_lds_dwordx4 v[18:19], off
	s_mov_b32 m0, s5
	ds_read_b128 v[178:181], v221 offset:8192
	ds_read_b128 v[170:173], v221 offset:8704
	ds_read_b128 v[174:177], v221 offset:10240
	ds_read_b128 v[162:165], v221 offset:10752
	ds_read_b128 v[166:169], v221 offset:12288
	ds_read_b128 v[154:157], v221 offset:12800
	ds_read_b128 v[158:161], v221 offset:14336
	ds_read_b128 v[150:153], v221 offset:14848
	v_exp_f32_e32 v34, v34
	v_exp_f32_e32 v35, v35
	v_exp_f32_e32 v20, v20
	v_exp_f32_e32 v21, v21
	v_exp_f32_e32 v22, v22
	v_exp_f32_e32 v23, v23
	v_exp_f32_e32 v24, v24
	v_exp_f32_e32 v25, v25
	v_exp_f32_e32 v26, v26
	v_exp_f32_e32 v27, v27
	v_exp_f32_e32 v28, v28
	v_exp_f32_e32 v29, v29
	v_exp_f32_e32 v30, v30
	v_exp_f32_e32 v31, v31
	v_exp_f32_e32 v32, v32
	v_exp_f32_e32 v33, v33
	s_waitcnt vmcnt(2) lgkmcnt(0)
	s_barrier
	v_and_b32_e32 v69, v68, v35
	v_and_b32_e32 v68, v67, v34
	v_bfe_i32 v34, v59, 31, 1
	v_and_b32_e32 v66, v100, v32
	v_and_b32_e32 v67, v34, v33
	v_and_b32_e32 v65, v99, v31
	v_and_b32_e32 v64, v98, v30
	v_and_b32_e32 v63, v97, v29
	v_and_b32_e32 v62, v96, v28
	v_and_b32_e32 v61, v95, v27
	v_and_b32_e32 v60, v94, v26
	v_and_b32_e32 v59, v93, v25
	v_and_b32_e32 v58, v92, v24
	v_and_b32_e32 v57, v91, v23
	v_and_b32_e32 v56, v90, v22
	v_and_b32_e32 v55, v89, v21
	v_and_b32_e32 v54, v88, v20
	s_cmp_lt_i32 s61, 7
	s_cbranch_scc1 .LBB0_1287
	s_mov_b64 s[4:5], 0x50000
	v_lshlrev_b32_e32 v18, 4, v214
	v_lshl_add_u64 v[188:189], v[194:195], 0, s[4:5]
	s_mov_b64 s[4:5], 0x300
	v_mov_b64_e32 v[34:35], v[16:17]
	v_lshl_add_u64 v[192:193], v[84:85], 0, s[4:5]
	v_add_u32_e32 v85, s57, v18
	v_mov_b64_e32 v[32:33], v[14:15]
	v_mov_b64_e32 v[30:31], v[12:13]
	v_mov_b64_e32 v[28:29], v[10:11]
	v_mov_b64_e32 v[26:27], v[8:9]
	v_mov_b64_e32 v[24:25], v[6:7]
	v_mov_b64_e32 v[22:23], v[4:5]
	v_mov_b64_e32 v[20:21], v[2:3]
	v_mov_b64_e32 v[18:19], v[16:17]
	s_add_i32 s46, s61, -5
	v_lshl_add_u32 v210, v213, 2, s57
	v_lshl_add_u64 v[190:191], v[208:209], 0, s[82:83]
	s_mov_b32 s4, 0
	s_movk_i32 s48, 0x4000
	s_movk_i32 s47, 0x2000
	v_mov_b32_e32 v84, 0
	v_mov_b64_e32 v[16:17], v[14:15]
	v_mov_b64_e32 v[14:15], v[12:13]
	v_mov_b64_e32 v[12:13], v[10:11]
	v_mov_b64_e32 v[10:11], v[8:9]
	v_mov_b64_e32 v[8:9], v[6:7]
	v_mov_b64_e32 v[6:7], v[4:5]
	v_mov_b64_e32 v[4:5], v[2:3]

.LBB0_1274:
	s_waitcnt lgkmcnt(0)
	v_and_b32_e32 v146, v146, v80
	v_and_b32_e32 v147, v147, v81
	v_and_b32_e32 v148, v148, v82
	v_and_b32_e32 v149, v149, v83
	ds_read_b128 v[80:83], v226 offset:51200
	s_waitcnt lgkmcnt(14)
	v_mfma_f32_32x32x16_bf16 v[20:35], v[146:149], v[182:185], v[20:35]
	v_exp_f32_e32 v102, v102
	v_exp_f32_e32 v103, v103
	v_exp_f32_e32 v104, v104
	v_exp_f32_e32 v105, v105
	s_waitcnt lgkmcnt(12)
	v_mfma_f32_32x32x16_bf16 v[4:19], v[146:149], v[178:181], v[4:19]
	v_mfma_f32_16x16x32_bf16 v[228:231], v[146:149], v[204:207], v[228:231]
	v_exp_f32_e32 v106, v106
	v_exp_f32_e32 v107, v107
	v_exp_f32_e32 v108, v108
	v_exp_f32_e32 v109, v109
	s_waitcnt lgkmcnt(0)
	v_and_b32_e32 v142, v142, v80
	v_and_b32_e32 v143, v143, v81
	v_and_b32_e32 v144, v144, v82
	v_and_b32_e32 v145, v145, v83
	ds_read_b128 v[80:83], v248 offset:51200
	v_add_u32_e32 v64, s48, v221
	ds_read_b128 v[60:63], v64
	ds_read_b128 v[150:153], v64 offset:512
	s_waitcnt lgkmcnt(12)
	v_mfma_f32_32x32x16_bf16 v[20:35], v[142:145], v[170:173], v[20:35]
	v_exp_f32_e32 v110, v110
	v_exp_f32_e32 v111, v111
	v_exp_f32_e32 v112, v112
	v_exp_f32_e32 v113, v113
	ds_read_b128 v[174:177], v64 offset:2048
	ds_read_b128 v[162:165], v64 offset:2560
	s_waitcnt lgkmcnt(12)
	v_mfma_f32_32x32x16_bf16 v[4:19], v[142:145], v[76:79], v[4:19]
	v_mfma_f32_16x16x32_bf16 v[228:231], v[142:145], v[204:207], v[228:231]
	v_exp_f32_e32 v114, v114
	v_exp_f32_e32 v115, v115
	v_exp_f32_e32 v116, v116
	v_exp_f32_e32 v117, v117
	s_waitcnt lgkmcnt(4)
	v_and_b32_e32 v130, v130, v80
	v_and_b32_e32 v131, v131, v81
	v_and_b32_e32 v132, v132, v82
	v_and_b32_e32 v133, v133, v83
	ds_read_b128 v[80:83], v249 offset:51200
	ds_read_b128 v[170:173], v64 offset:4096
	ds_read_b128 v[158:161], v64 offset:4608
	s_waitcnt lgkmcnt(12)
	v_mfma_f32_32x32x16_bf16 v[20:35], v[130:133], v[72:75], v[20:35]
	v_exp_f32_e32 v86, v86
	v_exp_f32_e32 v87, v87
	v_exp_f32_e32 v88, v88
	v_exp_f32_e32 v89, v89
	ds_read_b128 v[166:169], v64 offset:6144
	ds_read_b128 v[154:157], v64 offset:6656
	s_waitcnt lgkmcnt(12)
	v_mfma_f32_32x32x16_bf16 v[4:19], v[130:133], v[68:71], v[4:19]
	v_mfma_f32_16x16x32_bf16 v[228:231], v[130:133], v[204:207], v[228:231]
	v_exp_f32_e32 v90, v90
	v_exp_f32_e32 v91, v91
	v_exp_f32_e32 v92, v92
	v_exp_f32_e32 v93, v93
	s_waitcnt lgkmcnt(4)
	v_and_b32_e32 v118, v118, v80
	v_and_b32_e32 v119, v119, v81
	v_and_b32_e32 v120, v120, v82
	v_and_b32_e32 v121, v121, v83
	s_nop 0
	s_waitcnt lgkmcnt(10)
	v_mfma_f32_32x32x16_bf16 v[20:35], v[118:121], v[56:59], v[20:35]
	v_exp_f32_e32 v94, v94
	v_exp_f32_e32 v95, v95
	v_exp_f32_e32 v96, v96
	v_exp_f32_e32 v97, v97
	s_waitcnt lgkmcnt(8)
	v_mfma_f32_32x32x16_bf16 v[4:19], v[118:121], v[52:55], v[4:19]
	v_mfma_f32_16x16x32_bf16 v[228:231], v[118:121], v[204:207], v[228:231]
	v_exp_f32_e32 v98, v98
	v_exp_f32_e32 v99, v99
	v_exp_f32_e32 v100, v100
	v_exp_f32_e32 v101, v101
	v_lshlrev_b32_sdwa v225, s32, v218 dst_sel:DWORD dst_unused:UNUSED_PAD src0_sel:DWORD src1_sel:BYTE_0
	v_lshlrev_b32_sdwa v226, s32, v218 dst_sel:DWORD dst_unused:UNUSED_PAD src0_sel:DWORD src1_sel:BYTE_1
	v_lshlrev_b32_sdwa v248, s32, v218 dst_sel:DWORD dst_unused:UNUSED_PAD src0_sel:DWORD src1_sel:BYTE_2
	v_lshlrev_b32_sdwa v249, s32, v218 dst_sel:DWORD dst_unused:UNUSED_PAD src0_sel:DWORD src1_sel:BYTE_3
	s_waitcnt vmcnt(2) lgkmcnt(0)
	s_barrier
	s_andn2_b64 vcc, exec, s[42:43]
	s_cbranch_vccnz .LBB0_1276
	s_waitcnt lgkmcnt(0)
	ds_read_b128 v[52:55], v85 offset:49248
	ds_read_b128 v[56:59], v85 offset:49216
	ds_read_b128 v[64:67], v85 offset:49184
	ds_read_b128 v[68:71], v85 offset:49152
	s_waitcnt lgkmcnt(3)
	v_pk_mul_f32 v[32:33], v[32:33], v[52:53]
	s_waitcnt lgkmcnt(2)
	v_pk_mul_f32 v[28:29], v[28:29], v[56:57]
	s_waitcnt lgkmcnt(1)
	v_pk_mul_f32 v[24:25], v[24:25], v[64:65]
	v_pk_mul_f32 v[34:35], v[34:35], v[54:55]
	v_pk_mul_f32 v[30:31], v[30:31], v[58:59]
	v_pk_mul_f32 v[26:27], v[26:27], v[66:67]
	s_waitcnt lgkmcnt(0)
	v_pk_mul_f32 v[22:23], v[22:23], v[70:71]
	v_pk_mul_f32 v[20:21], v[20:21], v[68:69]
	v_pk_mul_f32 v[16:17], v[16:17], v[52:53]
	v_pk_mul_f32 v[12:13], v[12:13], v[56:57]
	v_pk_mul_f32 v[8:9], v[8:9], v[64:65]
	v_pk_mul_f32 v[18:19], v[18:19], v[54:55]
	v_pk_mul_f32 v[14:15], v[14:15], v[58:59]
	v_pk_mul_f32 v[10:11], v[10:11], v[66:67]
	v_pk_mul_f32 v[6:7], v[6:7], v[70:71]
	v_pk_mul_f32 v[4:5], v[4:5], v[68:69]
	ds_read_b128 v[240:243], v236 offset:49152
	s_waitcnt lgkmcnt(0)
	v_pk_mul_f32 v[228:229], v[228:229], v[240:241]
	v_pk_mul_f32 v[230:231], v[230:231], v[242:243]

.LBB0_1277:
	s_waitcnt lgkmcnt(0)
	v_and_b32_e32 v146, v146, v114
	v_and_b32_e32 v147, v147, v115
	v_and_b32_e32 v148, v148, v116
	v_and_b32_e32 v149, v149, v117
	ds_read_b128 v[114:117], v226 offset:51200
	s_waitcnt lgkmcnt(14)
	v_mfma_f32_32x32x16_bf16 v[20:35], v[146:149], v[182:185], v[20:35]
	v_exp_f32_e32 v68, v68
	v_exp_f32_e32 v69, v69
	v_exp_f32_e32 v70, v70
	v_exp_f32_e32 v71, v71
	s_waitcnt lgkmcnt(12)
	v_mfma_f32_32x32x16_bf16 v[4:19], v[146:149], v[178:181], v[4:19]
	v_mfma_f32_16x16x32_bf16 v[228:231], v[146:149], v[204:207], v[228:231]
	v_exp_f32_e32 v72, v72
	v_exp_f32_e32 v73, v73
	v_exp_f32_e32 v74, v74
	v_exp_f32_e32 v75, v75
	s_waitcnt lgkmcnt(0)
	v_and_b32_e32 v142, v142, v114
	v_and_b32_e32 v143, v143, v115
	v_and_b32_e32 v144, v144, v116
	v_and_b32_e32 v145, v145, v117
	ds_read_b128 v[114:117], v248 offset:51200
	v_add_u32_e32 v94, s60, v221
	ds_read_b128 v[178:181], v94
	ds_read_b128 v[170:173], v94 offset:512
	s_waitcnt lgkmcnt(12)
	v_mfma_f32_32x32x16_bf16 v[20:35], v[142:145], v[150:153], v[20:35]
	v_exp_f32_e32 v76, v76
	v_exp_f32_e32 v77, v77
	v_exp_f32_e32 v78, v78
	v_exp_f32_e32 v79, v79
	ds_read_b128 v[174:177], v94 offset:2048
	ds_read_b128 v[162:165], v94 offset:2560
	s_waitcnt lgkmcnt(12)
	v_mfma_f32_32x32x16_bf16 v[4:19], v[142:145], v[110:113], v[4:19]
	v_mfma_f32_16x16x32_bf16 v[228:231], v[142:145], v[204:207], v[228:231]
	v_exp_f32_e32 v80, v80
	v_exp_f32_e32 v81, v81
	v_exp_f32_e32 v82, v82
	v_exp_f32_e32 v83, v83
	s_waitcnt lgkmcnt(4)
	v_and_b32_e32 v130, v130, v114
	v_and_b32_e32 v131, v131, v115
	v_and_b32_e32 v132, v132, v116
	v_and_b32_e32 v133, v133, v117
	ds_read_b128 v[114:117], v249 offset:51200
	ds_read_b128 v[166:169], v94 offset:4096
	ds_read_b128 v[154:157], v94 offset:4608
	s_waitcnt lgkmcnt(12)
	v_mfma_f32_32x32x16_bf16 v[20:35], v[130:133], v[106:109], v[20:35]
	v_exp_f32_e32 v52, v52
	v_exp_f32_e32 v53, v53
	v_exp_f32_e32 v54, v54
	v_exp_f32_e32 v55, v55
	ds_read_b128 v[158:161], v94 offset:6144
	ds_read_b128 v[150:153], v94 offset:6656
	s_waitcnt lgkmcnt(12)
	v_mfma_f32_32x32x16_bf16 v[4:19], v[130:133], v[102:105], v[4:19]
	v_mfma_f32_16x16x32_bf16 v[228:231], v[130:133], v[204:207], v[228:231]
	v_exp_f32_e32 v56, v56
	v_exp_f32_e32 v57, v57
	v_exp_f32_e32 v58, v58
	v_exp_f32_e32 v59, v59
	s_waitcnt lgkmcnt(4)
	v_and_b32_e32 v118, v118, v114
	v_and_b32_e32 v119, v119, v115
	v_and_b32_e32 v120, v120, v116
	v_and_b32_e32 v121, v121, v117
	s_nop 0
	s_waitcnt lgkmcnt(10)
	v_mfma_f32_32x32x16_bf16 v[20:35], v[118:121], v[90:93], v[20:35]
	v_exp_f32_e32 v60, v60
	v_exp_f32_e32 v61, v61
	v_exp_f32_e32 v62, v62
	v_exp_f32_e32 v63, v63
	s_waitcnt lgkmcnt(8)
	v_mfma_f32_32x32x16_bf16 v[4:19], v[118:121], v[86:89], v[4:19]
	v_mfma_f32_16x16x32_bf16 v[228:231], v[118:121], v[204:207], v[228:231]
	v_exp_f32_e32 v64, v64
	v_exp_f32_e32 v65, v65
	v_exp_f32_e32 v66, v66
	v_exp_f32_e32 v67, v67
	v_lshlrev_b32_sdwa v225, s32, v2 dst_sel:DWORD dst_unused:UNUSED_PAD src0_sel:DWORD src1_sel:BYTE_0
	v_lshlrev_b32_sdwa v226, s32, v2 dst_sel:DWORD dst_unused:UNUSED_PAD src0_sel:DWORD src1_sel:BYTE_1
	v_lshlrev_b32_sdwa v248, s32, v2 dst_sel:DWORD dst_unused:UNUSED_PAD src0_sel:DWORD src1_sel:BYTE_2
	v_lshlrev_b32_sdwa v249, s32, v2 dst_sel:DWORD dst_unused:UNUSED_PAD src0_sel:DWORD src1_sel:BYTE_3
	s_waitcnt vmcnt(2) lgkmcnt(0)
	s_barrier
	s_andn2_b64 vcc, exec, s[42:43]
	s_cbranch_vccnz .LBB0_1279
	s_waitcnt lgkmcnt(0)
	ds_read_b128 v[86:89], v85 offset:49248
	ds_read_b128 v[90:93], v85 offset:49216
	ds_read_b128 v[94:97], v85 offset:49184
	ds_read_b128 v[98:101], v85 offset:49152
	s_waitcnt lgkmcnt(3)
	v_pk_mul_f32 v[32:33], v[32:33], v[86:87]
	s_waitcnt lgkmcnt(2)
	v_pk_mul_f32 v[28:29], v[28:29], v[90:91]
	s_waitcnt lgkmcnt(1)
	v_pk_mul_f32 v[24:25], v[24:25], v[94:95]
	v_pk_mul_f32 v[34:35], v[34:35], v[88:89]
	v_pk_mul_f32 v[30:31], v[30:31], v[92:93]
	v_pk_mul_f32 v[26:27], v[26:27], v[96:97]
	s_waitcnt lgkmcnt(0)
	v_pk_mul_f32 v[22:23], v[22:23], v[100:101]
	v_pk_mul_f32 v[20:21], v[20:21], v[98:99]
	v_pk_mul_f32 v[16:17], v[16:17], v[86:87]
	v_pk_mul_f32 v[12:13], v[12:13], v[90:91]
	v_pk_mul_f32 v[8:9], v[8:9], v[94:95]
	v_pk_mul_f32 v[18:19], v[18:19], v[88:89]
	v_pk_mul_f32 v[14:15], v[14:15], v[92:93]
	v_pk_mul_f32 v[10:11], v[10:11], v[96:97]
	v_pk_mul_f32 v[6:7], v[6:7], v[100:101]
	v_pk_mul_f32 v[4:5], v[4:5], v[98:99]
	ds_read_b128 v[240:243], v236 offset:49152
	s_waitcnt lgkmcnt(0)
	v_pk_mul_f32 v[228:229], v[228:229], v[240:241]
	v_pk_mul_f32 v[230:231], v[230:231], v[242:243]

.LBB0_1293:
	s_waitcnt lgkmcnt(0)
	v_and_b32_e32 v146, v146, v80
	v_and_b32_e32 v147, v147, v81
	v_and_b32_e32 v148, v148, v82
	v_and_b32_e32 v149, v149, v83
	ds_read_b128 v[80:83], v226 offset:51200
	s_waitcnt lgkmcnt(14)
	v_mfma_f32_32x32x16_bf16 v[20:35], v[146:149], v[186:189], v[20:35]
	v_exp_f32_e32 v102, v102
	v_exp_f32_e32 v103, v103
	v_exp_f32_e32 v104, v104
	v_exp_f32_e32 v105, v105
	s_waitcnt lgkmcnt(12)
	v_mfma_f32_32x32x16_bf16 v[4:19], v[146:149], v[178:181], v[4:19]
	v_mfma_f32_16x16x32_bf16 v[228:231], v[146:149], v[204:207], v[228:231]
	v_exp_f32_e32 v106, v106
	v_exp_f32_e32 v107, v107
	v_exp_f32_e32 v108, v108
	v_exp_f32_e32 v109, v109
	s_waitcnt lgkmcnt(0)
	v_and_b32_e32 v142, v142, v80
	v_and_b32_e32 v143, v143, v81
	v_and_b32_e32 v144, v144, v82
	v_and_b32_e32 v145, v145, v83
	ds_read_b128 v[80:83], v248 offset:51200
	v_add_u32_e32 v60, s62, v221
	ds_read_b128 v[178:181], v60
	ds_read_b128 v[170:173], v60 offset:512
	s_waitcnt lgkmcnt(12)
	v_mfma_f32_32x32x16_bf16 v[20:35], v[142:145], v[182:185], v[20:35]
	v_exp_f32_e32 v110, v110
	v_exp_f32_e32 v111, v111
	v_exp_f32_e32 v112, v112
	v_exp_f32_e32 v113, v113
	ds_read_b128 v[174:177], v60 offset:2048
	ds_read_b128 v[162:165], v60 offset:2560
	s_waitcnt lgkmcnt(12)
	v_mfma_f32_32x32x16_bf16 v[4:19], v[142:145], v[76:79], v[4:19]
	v_mfma_f32_16x16x32_bf16 v[228:231], v[142:145], v[204:207], v[228:231]
	v_exp_f32_e32 v114, v114
	v_exp_f32_e32 v115, v115
	v_exp_f32_e32 v116, v116
	v_exp_f32_e32 v117, v117
	s_waitcnt lgkmcnt(4)
	v_and_b32_e32 v130, v130, v80
	v_and_b32_e32 v131, v131, v81
	v_and_b32_e32 v132, v132, v82
	v_and_b32_e32 v133, v133, v83
	ds_read_b128 v[80:83], v249 offset:51200
	ds_read_b128 v[166:169], v60 offset:4096
	ds_read_b128 v[154:157], v60 offset:4608
	s_waitcnt lgkmcnt(12)
	v_mfma_f32_32x32x16_bf16 v[20:35], v[130:133], v[72:75], v[20:35]
	v_exp_f32_e32 v86, v86
	v_exp_f32_e32 v87, v87
	v_exp_f32_e32 v88, v88
	v_exp_f32_e32 v89, v89
	ds_read_b128 v[158:161], v60 offset:6144
	ds_read_b128 v[150:153], v60 offset:6656
	s_waitcnt lgkmcnt(12)
	v_mfma_f32_32x32x16_bf16 v[4:19], v[130:133], v[68:71], v[4:19]
	v_mfma_f32_16x16x32_bf16 v[228:231], v[130:133], v[204:207], v[228:231]
	v_exp_f32_e32 v90, v90
	v_exp_f32_e32 v91, v91
	v_exp_f32_e32 v92, v92
	v_exp_f32_e32 v93, v93
	s_waitcnt lgkmcnt(4)
	v_and_b32_e32 v118, v118, v80
	v_and_b32_e32 v119, v119, v81
	v_and_b32_e32 v120, v120, v82
	v_and_b32_e32 v121, v121, v83
	s_nop 0
	s_waitcnt lgkmcnt(10)
	v_mfma_f32_32x32x16_bf16 v[20:35], v[118:121], v[56:59], v[20:35]
	v_exp_f32_e32 v94, v94
	v_exp_f32_e32 v95, v95
	v_exp_f32_e32 v96, v96
	v_exp_f32_e32 v97, v97
	s_waitcnt lgkmcnt(8)
	v_mfma_f32_32x32x16_bf16 v[4:19], v[118:121], v[52:55], v[4:19]
	v_mfma_f32_16x16x32_bf16 v[228:231], v[118:121], v[204:207], v[228:231]
	v_exp_f32_e32 v98, v98
	v_exp_f32_e32 v99, v99
	v_exp_f32_e32 v100, v100
	v_exp_f32_e32 v101, v101
	v_lshlrev_b32_sdwa v225, s32, v218 dst_sel:DWORD dst_unused:UNUSED_PAD src0_sel:DWORD src1_sel:BYTE_0
	v_lshlrev_b32_sdwa v226, s32, v218 dst_sel:DWORD dst_unused:UNUSED_PAD src0_sel:DWORD src1_sel:BYTE_1
	v_lshlrev_b32_sdwa v248, s32, v218 dst_sel:DWORD dst_unused:UNUSED_PAD src0_sel:DWORD src1_sel:BYTE_2
	v_lshlrev_b32_sdwa v249, s32, v218 dst_sel:DWORD dst_unused:UNUSED_PAD src0_sel:DWORD src1_sel:BYTE_3
	s_mov_b64 s[4:5], -1
	s_and_b64 vcc, exec, s[48:49]
	s_cbranch_vccnz .LBB0_1318
	s_andn2_b64 vcc, exec, s[4:5]
	s_cbranch_vccz .LBB0_1323

.LBB0_1296:
	s_waitcnt lgkmcnt(0)
	ds_read_b128 v[52:55], v222 offset:49248
	ds_read_b128 v[56:59], v222 offset:49216
	ds_read_b128 v[60:63], v222 offset:49184
	ds_read_b128 v[64:67], v222 offset:49152
	s_waitcnt lgkmcnt(3)
	v_pk_mul_f32 v[32:33], v[32:33], v[52:53]
	s_waitcnt lgkmcnt(2)
	v_pk_mul_f32 v[28:29], v[28:29], v[56:57]
	s_waitcnt lgkmcnt(1)
	v_pk_mul_f32 v[24:25], v[24:25], v[60:61]
	v_pk_mul_f32 v[34:35], v[34:35], v[54:55]
	v_pk_mul_f32 v[30:31], v[30:31], v[58:59]
	v_pk_mul_f32 v[26:27], v[26:27], v[62:63]
	s_waitcnt lgkmcnt(0)
	v_pk_mul_f32 v[22:23], v[22:23], v[66:67]
	v_pk_mul_f32 v[20:21], v[20:21], v[64:65]
	v_pk_mul_f32 v[16:17], v[16:17], v[52:53]
	v_pk_mul_f32 v[12:13], v[12:13], v[56:57]
	v_pk_mul_f32 v[8:9], v[8:9], v[60:61]
	v_pk_mul_f32 v[18:19], v[18:19], v[54:55]
	v_pk_mul_f32 v[14:15], v[14:15], v[58:59]
	v_pk_mul_f32 v[10:11], v[10:11], v[62:63]
	v_pk_mul_f32 v[6:7], v[6:7], v[66:67]
	v_pk_mul_f32 v[4:5], v[4:5], v[64:65]
	ds_read_b128 v[240:243], v236 offset:49152
	s_waitcnt lgkmcnt(0)
	v_pk_mul_f32 v[228:229], v[228:229], v[240:241]
	v_pk_mul_f32 v[230:231], v[230:231], v[242:243]

.LBB0_1304:
	s_waitcnt lgkmcnt(0)
	v_and_b32_e32 v146, v146, v114
	v_and_b32_e32 v147, v147, v115
	v_and_b32_e32 v148, v148, v116
	v_and_b32_e32 v149, v149, v117
	ds_read_b128 v[114:117], v226 offset:51200
	s_waitcnt lgkmcnt(14)
	v_mfma_f32_32x32x16_bf16 v[20:35], v[146:149], v[190:193], v[20:35]
	v_exp_f32_e32 v68, v68
	v_exp_f32_e32 v69, v69
	v_exp_f32_e32 v70, v70
	v_exp_f32_e32 v71, v71
	s_waitcnt lgkmcnt(12)
	v_mfma_f32_32x32x16_bf16 v[4:19], v[146:149], v[186:189], v[4:19]
	v_mfma_f32_16x16x32_bf16 v[228:231], v[146:149], v[204:207], v[228:231]
	v_exp_f32_e32 v72, v72
	v_exp_f32_e32 v73, v73
	v_exp_f32_e32 v74, v74
	v_exp_f32_e32 v75, v75
	s_waitcnt lgkmcnt(0)
	v_and_b32_e32 v142, v142, v114
	v_and_b32_e32 v143, v143, v115
	v_and_b32_e32 v144, v144, v116
	v_and_b32_e32 v145, v145, v117
	ds_read_b128 v[114:117], v248 offset:51200
	s_and_b64 vcc, exec, s[42:43]
	s_cbranch_vccnz .LBB0_1306
	v_add_u32_e32 v85, s60, v221
	ds_read_b128 v[178:181], v85
	ds_read_b128 v[170:173], v85 offset:512

.LBB0_1308:
	s_waitcnt lgkmcnt(8)
	v_mfma_f32_32x32x16_bf16 v[4:19], v[142:145], v[110:113], v[4:19]
	v_mfma_f32_16x16x32_bf16 v[228:231], v[142:145], v[204:207], v[228:231]
	v_exp_f32_e32 v80, v80
	v_exp_f32_e32 v81, v81
	v_exp_f32_e32 v82, v82
	v_exp_f32_e32 v83, v83
	s_waitcnt lgkmcnt(0)
	v_and_b32_e32 v130, v130, v114
	v_and_b32_e32 v131, v131, v115
	v_and_b32_e32 v132, v132, v116
	v_and_b32_e32 v133, v133, v117
	ds_read_b128 v[114:117], v249 offset:51200
	s_and_b64 vcc, exec, s[42:43]
	s_cbranch_vccnz .LBB0_1310
	v_add_u32_e32 v85, s60, v221
	ds_read_b128 v[166:169], v85 offset:4096
	ds_read_b128 v[154:157], v85 offset:4608

.LBB0_1312:
	s_waitcnt lgkmcnt(4)
	v_mfma_f32_32x32x16_bf16 v[4:19], v[130:133], v[102:105], v[4:19]
	v_mfma_f32_16x16x32_bf16 v[228:231], v[130:133], v[204:207], v[228:231]
	v_exp_f32_e32 v56, v56
	v_exp_f32_e32 v57, v57
	v_exp_f32_e32 v58, v58
	v_exp_f32_e32 v59, v59
	s_waitcnt lgkmcnt(0)
	v_and_b32_e32 v118, v118, v114
	v_and_b32_e32 v119, v119, v115
	v_and_b32_e32 v120, v120, v116
	v_and_b32_e32 v121, v121, v117
	s_nop 0
	s_waitcnt lgkmcnt(2)
	v_mfma_f32_32x32x16_bf16 v[20:35], v[118:121], v[90:93], v[20:35]
	v_exp_f32_e32 v60, v60
	v_exp_f32_e32 v61, v61
	v_exp_f32_e32 v62, v62
	v_exp_f32_e32 v63, v63
	s_waitcnt lgkmcnt(0)
	v_mfma_f32_32x32x16_bf16 v[4:19], v[118:121], v[86:89], v[4:19]
	v_mfma_f32_16x16x32_bf16 v[228:231], v[118:121], v[204:207], v[228:231]
	v_exp_f32_e32 v64, v64
	v_exp_f32_e32 v65, v65
	v_exp_f32_e32 v66, v66
	v_exp_f32_e32 v67, v67
	v_lshlrev_b32_sdwa v225, s32, v223 dst_sel:DWORD dst_unused:UNUSED_PAD src0_sel:DWORD src1_sel:BYTE_0
	v_lshlrev_b32_sdwa v226, s32, v223 dst_sel:DWORD dst_unused:UNUSED_PAD src0_sel:DWORD src1_sel:BYTE_1
	v_lshlrev_b32_sdwa v248, s32, v223 dst_sel:DWORD dst_unused:UNUSED_PAD src0_sel:DWORD src1_sel:BYTE_2
	v_lshlrev_b32_sdwa v249, s32, v223 dst_sel:DWORD dst_unused:UNUSED_PAD src0_sel:DWORD src1_sel:BYTE_3
	s_mov_b64 s[4:5], -1
	s_and_b64 vcc, exec, s[50:51]
	s_cbranch_vccnz .LBB0_1324
	s_andn2_b64 vcc, exec, s[4:5]
	s_cbranch_vccz .LBB0_1329

.LBB0_1315:
	s_waitcnt lgkmcnt(0)
	ds_read_b128 v[86:89], v222 offset:49248
	ds_read_b128 v[90:93], v222 offset:49216
	ds_read_b128 v[94:97], v222 offset:49184
	ds_read_b128 v[98:101], v222 offset:49152
	s_waitcnt lgkmcnt(3)
	v_pk_mul_f32 v[32:33], v[32:33], v[86:87]
	s_waitcnt lgkmcnt(2)
	v_pk_mul_f32 v[28:29], v[28:29], v[90:91]
	s_waitcnt lgkmcnt(1)
	v_pk_mul_f32 v[24:25], v[24:25], v[94:95]
	v_pk_mul_f32 v[34:35], v[34:35], v[88:89]
	v_pk_mul_f32 v[30:31], v[30:31], v[92:93]
	v_pk_mul_f32 v[26:27], v[26:27], v[96:97]
	s_waitcnt lgkmcnt(0)
	v_pk_mul_f32 v[22:23], v[22:23], v[100:101]
	v_pk_mul_f32 v[20:21], v[20:21], v[98:99]
	v_pk_mul_f32 v[16:17], v[16:17], v[86:87]
	v_pk_mul_f32 v[12:13], v[12:13], v[90:91]
	v_pk_mul_f32 v[8:9], v[8:9], v[94:95]
	v_pk_mul_f32 v[18:19], v[18:19], v[88:89]
	v_pk_mul_f32 v[14:15], v[14:15], v[92:93]
	v_pk_mul_f32 v[10:11], v[10:11], v[96:97]
	v_pk_mul_f32 v[6:7], v[6:7], v[100:101]
	v_pk_mul_f32 v[4:5], v[4:5], v[98:99]
	ds_read_b128 v[240:243], v236 offset:49152
	s_waitcnt lgkmcnt(0)
	v_pk_mul_f32 v[228:229], v[228:229], v[240:241]
	v_pk_mul_f32 v[230:231], v[230:231], v[242:243]

.LBB0_1338:
	s_waitcnt lgkmcnt(0)
	v_and_b32_e32 v146, v146, v154
	v_and_b32_e32 v147, v147, v155
	v_and_b32_e32 v148, v148, v156
	v_and_b32_e32 v149, v149, v157
	ds_read_b128 v[154:157], v226 offset:51200
	s_waitcnt lgkmcnt(14)
	v_mfma_f32_32x32x16_bf16 v[20:35], v[146:149], v[114:117], v[20:35]
	v_exp_f32_e32 v86, v86
	v_exp_f32_e32 v87, v87
	v_exp_f32_e32 v88, v88
	v_exp_f32_e32 v89, v89
	s_waitcnt lgkmcnt(12)
	v_mfma_f32_32x32x16_bf16 v[4:19], v[146:149], v[110:113], v[4:19]
	v_mfma_f32_16x16x32_bf16 v[228:231], v[146:149], v[204:207], v[228:231]
	v_exp_f32_e32 v90, v90
	v_exp_f32_e32 v91, v91
	v_exp_f32_e32 v92, v92
	v_exp_f32_e32 v93, v93
	s_waitcnt lgkmcnt(0)
	v_and_b32_e32 v142, v142, v154
	v_and_b32_e32 v143, v143, v155
	v_and_b32_e32 v144, v144, v156
	v_and_b32_e32 v145, v145, v157
	ds_read_b128 v[154:157], v248 offset:51200
	s_waitcnt lgkmcnt(10)
	v_mfma_f32_32x32x16_bf16 v[20:35], v[142:145], v[106:109], v[20:35]
	v_exp_f32_e32 v94, v94
	v_exp_f32_e32 v95, v95
	v_exp_f32_e32 v96, v96
	v_exp_f32_e32 v97, v97
	s_waitcnt lgkmcnt(8)
	v_mfma_f32_32x32x16_bf16 v[4:19], v[142:145], v[102:105], v[4:19]
	v_mfma_f32_16x16x32_bf16 v[228:231], v[142:145], v[204:207], v[228:231]
	v_exp_f32_e32 v98, v98
	v_exp_f32_e32 v99, v99
	v_exp_f32_e32 v100, v100
	v_exp_f32_e32 v101, v101
	s_waitcnt lgkmcnt(0)
	v_and_b32_e32 v130, v130, v154
	v_and_b32_e32 v131, v131, v155
	v_and_b32_e32 v132, v132, v156
	v_and_b32_e32 v133, v133, v157
	ds_read_b128 v[154:157], v249 offset:51200
	s_waitcnt lgkmcnt(6)
	v_mfma_f32_32x32x16_bf16 v[20:35], v[130:133], v[80:83], v[20:35]
	v_exp_f32_e32 v36, v36
	v_exp_f32_e32 v37, v37
	v_exp_f32_e32 v38, v38
	v_exp_f32_e32 v39, v39
	s_waitcnt lgkmcnt(4)
	v_mfma_f32_32x32x16_bf16 v[4:19], v[130:133], v[76:79], v[4:19]
	v_mfma_f32_16x16x32_bf16 v[228:231], v[130:133], v[204:207], v[228:231]
	v_exp_f32_e32 v40, v40
	v_exp_f32_e32 v41, v41
	v_exp_f32_e32 v42, v42
	v_exp_f32_e32 v43, v43
	s_waitcnt lgkmcnt(0)
	v_and_b32_e32 v118, v118, v154
	v_and_b32_e32 v119, v119, v155
	v_and_b32_e32 v120, v120, v156
	v_and_b32_e32 v121, v121, v157
	s_nop 0
	s_waitcnt lgkmcnt(2)
	v_mfma_f32_32x32x16_bf16 v[20:35], v[118:121], v[72:75], v[20:35]
	v_exp_f32_e32 v44, v44
	v_exp_f32_e32 v45, v45
	v_exp_f32_e32 v46, v46
	v_exp_f32_e32 v47, v47
	s_waitcnt lgkmcnt(0)
	v_mfma_f32_32x32x16_bf16 v[4:19], v[118:121], v[68:71], v[4:19]
	v_mfma_f32_16x16x32_bf16 v[228:231], v[118:121], v[204:207], v[228:231]
	v_exp_f32_e32 v48, v48
	v_exp_f32_e32 v49, v49
	v_exp_f32_e32 v50, v50
	v_exp_f32_e32 v51, v51
	v_lshlrev_b32_sdwa v225, s32, v218 dst_sel:DWORD dst_unused:UNUSED_PAD src0_sel:DWORD src1_sel:BYTE_0
	v_lshlrev_b32_sdwa v226, s32, v218 dst_sel:DWORD dst_unused:UNUSED_PAD src0_sel:DWORD src1_sel:BYTE_1
	v_lshlrev_b32_sdwa v248, s32, v218 dst_sel:DWORD dst_unused:UNUSED_PAD src0_sel:DWORD src1_sel:BYTE_2
	v_lshlrev_b32_sdwa v249, s32, v218 dst_sel:DWORD dst_unused:UNUSED_PAD src0_sel:DWORD src1_sel:BYTE_3
	s_andn2_b64 vcc, exec, s[40:41]
	v_lshl_add_u32 v52, v214, 4, s57
	s_cbranch_vccnz .LBB0_1340
	s_waitcnt lgkmcnt(0)
	ds_read_b128 v[54:57], v52 offset:49248
	ds_read_b128 v[58:61], v52 offset:49216
	ds_read_b128 v[62:65], v52 offset:49184
	ds_read_b128 v[66:69], v52 offset:49152
	s_waitcnt lgkmcnt(3)
	v_pk_mul_f32 v[34:35], v[34:35], v[56:57]
	s_waitcnt lgkmcnt(2)
	v_pk_mul_f32 v[30:31], v[30:31], v[60:61]
	s_waitcnt lgkmcnt(1)
	v_pk_mul_f32 v[26:27], v[26:27], v[64:65]
	s_waitcnt lgkmcnt(0)
	v_pk_mul_f32 v[22:23], v[22:23], v[68:69]
	v_pk_mul_f32 v[32:33], v[32:33], v[54:55]
	v_pk_mul_f32 v[28:29], v[28:29], v[58:59]
	v_pk_mul_f32 v[24:25], v[24:25], v[62:63]
	v_pk_mul_f32 v[20:21], v[20:21], v[66:67]
	v_pk_mul_f32 v[18:19], v[18:19], v[56:57]
	v_pk_mul_f32 v[14:15], v[14:15], v[60:61]
	v_pk_mul_f32 v[10:11], v[10:11], v[64:65]
	v_pk_mul_f32 v[6:7], v[6:7], v[68:69]
	v_pk_mul_f32 v[16:17], v[16:17], v[54:55]
	v_pk_mul_f32 v[12:13], v[12:13], v[58:59]
	v_pk_mul_f32 v[8:9], v[8:9], v[62:63]
	v_pk_mul_f32 v[4:5], v[4:5], v[66:67]
	ds_read_b128 v[240:243], v236 offset:49152
	s_waitcnt lgkmcnt(0)
	v_pk_mul_f32 v[228:229], v[228:229], v[240:241]
	v_pk_mul_f32 v[230:231], v[230:231], v[242:243]
; #define SBAR() __builtin_amdgcn_sched_barrier(0)
;   #define RESC() do{ if(resc){ asm volatile("s_waitcnt lgkmcnt(0)":::"memory"); \
;       _Pragma("unroll") for(int d_=0;d_<2;++d_) _Pragma("unroll") for(int r=0;r<16;++r)o[d_][r]*=wsf[crow(r,hi)]; } }while(0)
;   #define PKW(P,B) cvtpk_s(P[B],P[B+1])
; __device__ __forceinline__ void pv(f32x16*o,int vb,bf16x8 pa0,bf16x8 pa1,bf16x8 pa2,bf16x8 pa3){
;   #pragma unroll
;   for(int d0=0;d0<2;++d0){s16x4 lo[4],hi[4];
;     #pragma unroll
;     for(int ks=0;ks<4;++ks){
;       asm volatile("ds_read_b64_tr_b16 %0,%1 offset:%c2":"=&v"(lo[ks]):"v"(vb),"i"(d0*4096+ks*1024):"memory");
;       asm volatile("ds_read_b64_tr_b16 %0,%1 offset:%c2":"=&v"(hi[ks]):"v"(vb),"i"(d0*4096+ks*1024+512):"memory");}
;     asm volatile("s_waitcnt lgkmcnt(0)":::"memory");SBAR();
;     ...
;     o[d0]=__builtin_amdgcn_mfma_f32_32x32x16_bf16(pa0,PK(0),o[d0],0,0,0);
;     o[d0]=__builtin_amdgcn_mfma_f32_32x32x16_bf16(pa1,PK(1),o[d0],0,0,0);
;     o[d0]=__builtin_amdgcn_mfma_f32_32x32x16_bf16(pa2,PK(2),o[d0],0,0,0);
;     o[d0]=__builtin_amdgcn_mfma_f32_32x32x16_bf16(pa3,PK(3),o[d0],0,0,0);
;     ...
;   }
; }
; template<int THRL> __device__ __forceinline__ void attn_unit(int b,int h,int qb,const bf16*Q,const bf16*__restrict__ K,const bf16*__restrict__ V,bf16*O,const unsigned*MASK,char*shm){
;     ...
;   STEP(pB0,pB1,pA0,pA1,NT-1,false,false,false,wB,wA); RESC();
;   { float sacc=pB0[0]+pB0[1]; _Pragma("unroll") for(int r=2;r<16;++r)sacc+=pB0[r]; _Pragma("unroll") for(int r=0;r<16;++r)sacc+=pB1[r]; l_reg+=sacc;
;     pw0=(u32x4){PKW(pB0,0),PKW(pB0,2),PKW(pB0,4),PKW(pB0,6)};pw1=(u32x4){PKW(pB0,8),PKW(pB0,10),PKW(pB0,12),PKW(pB0,14)};pw2=(u32x4){PKW(pB1,0),PKW(pB1,2),PKW(pB1,4),PKW(pB1,6)};pw3=(u32x4){PKW(pB1,8),PKW(pB1,10),PKW(pB1,12),PKW(pB1,14)};
;     SBAR(); pv(o,vb0+sl_cur,PAF(0),PAF(1),PAF(2),PAF(3)); }
;     ...
;   {auto rr=__builtin_amdgcn_permlane32_swap(__float_as_uint(l_reg),__float_as_uint(l_reg),false,false);l_reg=__uint_as_float(rr[0])+__uint_as_float(rr[1]);}
;   if(hi==0)wsf[32+r32]=l_reg;asm volatile("s_waitcnt lgkmcnt(0)":::"memory");
.LBB0_1340:
	s_cmp_lg_u32 0, -1
	s_cselect_b32 s4, 0, 0
	s_addk_i32 s4, 0x6000
	v_cvt_pk_bf16_f32 v36, v36, v37
	v_add3_u32 v53, v217, s4, v215
	v_cvt_pk_bf16_f32 v54, v86, v87
	v_cvt_pk_bf16_f32 v55, v88, v89
	v_cvt_pk_bf16_f32 v56, v90, v91
	v_cvt_pk_bf16_f32 v57, v92, v93
	v_cvt_pk_bf16_f32 v58, v94, v95
	v_cvt_pk_bf16_f32 v59, v96, v97
	v_cvt_pk_bf16_f32 v60, v98, v99
	v_cvt_pk_bf16_f32 v61, v100, v101
	v_cvt_pk_bf16_f32 v37, v38, v39
	v_cvt_pk_bf16_f32 v38, v40, v41
	v_cvt_pk_bf16_f32 v39, v42, v43
	v_cvt_pk_bf16_f32 v40, v44, v45
	v_cvt_pk_bf16_f32 v41, v46, v47
	v_cvt_pk_bf16_f32 v42, v48, v49
	v_cvt_pk_bf16_f32 v43, v50, v51
	ds_read_b128 v[86:89], v225 offset:51200
	ds_read_b128 v[90:93], v226 offset:51200
	ds_read_b128 v[94:97], v248 offset:51200
	ds_read_b128 v[98:101], v249 offset:51200
	v_add3_u32 v53, v53, v216, s60
	ds_read_b64_tr_b16 v[44:45],v53 offset:0
	ds_read_b64_tr_b16 v[46:47],v53 offset:512
	ds_read_b64_tr_b16 v[48:49],v53 offset:1024
	ds_read_b64_tr_b16 v[50:51],v53 offset:1536
	ds_read_b64_tr_b16 v[62:63],v53 offset:2048
	ds_read_b64_tr_b16 v[64:65],v53 offset:2560
	ds_read_b64_tr_b16 v[66:67],v53 offset:3072
	ds_read_b64_tr_b16 v[68:69],v53 offset:3584
	s_waitcnt lgkmcnt(0)
	v_and_b32_e32 v54, v54, v86
	v_and_b32_e32 v55, v55, v87
	v_and_b32_e32 v56, v56, v88
	v_and_b32_e32 v57, v57, v89
	v_and_b32_e32 v58, v58, v90
	v_and_b32_e32 v59, v59, v91
	v_and_b32_e32 v60, v60, v92
	v_and_b32_e32 v61, v61, v93
	v_and_b32_e32 v36, v36, v94
	v_and_b32_e32 v37, v37, v95
	v_and_b32_e32 v38, v38, v96
	v_and_b32_e32 v39, v39, v97
	v_and_b32_e32 v40, v40, v98
	v_and_b32_e32 v41, v41, v99
	v_and_b32_e32 v42, v42, v100
	v_and_b32_e32 v43, v43, v101
	s_nop 0
	v_mfma_f32_32x32x16_bf16 v[20:35], v[54:57], v[44:47], v[20:35]
	ds_read_b64_tr_b16 v[44:45],v53 offset:4096
	ds_read_b64_tr_b16 v[46:47],v53 offset:4608
	v_mfma_f32_32x32x16_bf16 v[20:35], v[58:61], v[48:51], v[20:35]
	ds_read_b64_tr_b16 v[48:49],v53 offset:5120
	ds_read_b64_tr_b16 v[50:51],v53 offset:5632
	v_mfma_f32_32x32x16_bf16 v[20:35], v[36:39], v[62:65], v[20:35]
	ds_read_b64_tr_b16 v[62:63],v53 offset:6144
	ds_read_b64_tr_b16 v[64:65],v53 offset:6656
	v_mfma_f32_32x32x16_bf16 v[20:35], v[40:43], v[66:69], v[20:35]
	v_mfma_f32_16x16x32_bf16 v[228:231], v[54:57], v[204:207], v[228:231]
	v_mfma_f32_16x16x32_bf16 v[228:231], v[58:61], v[204:207], v[228:231]
	v_mfma_f32_16x16x32_bf16 v[228:231], v[36:39], v[204:207], v[228:231]
	v_mfma_f32_16x16x32_bf16 v[228:231], v[40:43], v[204:207], v[228:231]
	ds_read_b64_tr_b16 v[66:67],v53 offset:7168
	ds_read_b64_tr_b16 v[68:69],v53 offset:7680
	s_waitcnt lgkmcnt(0)
	v_mfma_f32_32x32x16_bf16 v[4:19], v[54:57], v[44:47], v[4:19]
	v_and_b32_e32 v237, 15, v1
	v_cmp_gt_u32_e32 vcc, 2, v237
	v_mfma_f32_32x32x16_bf16 v[4:19], v[58:61], v[48:51], v[4:19]
	v_mfma_f32_32x32x16_bf16 v[4:19], v[36:39], v[62:65], v[4:19]
	s_nop 1
	v_mfma_f32_32x32x16_bf16 v[4:19], v[40:43], v[66:69], v[4:19]
	s_and_saveexec_b64 s[4:5], vcc
	s_cbranch_execz .LBB0_1260
	ds_write_b128 v236, v[228:231] offset:49280
	s_branch .LBB0_1260
